# scores section regenerated: all q'/key fragment addresses from 8 base regs + immediates, up to 15 LDS reads in flight ahead of the MFMA chain
# baseline (speedup 1.0000x reference)
_Z7na_mainPKDF16_PKhS0_PKfS4_S4_S4_Pf:
	s_lshl_b32 s3, s2, 5
	s_and_b32 s3, s3, 0xe0
	s_ashr_i32 s2, s2, 3
	s_add_i32 s3, s3, s2
	s_ashr_i32 s2, s3, 6
	s_lshl_b32 s3, s3, 5
	s_and_b32 s14, s3, 0x7e0
	v_mov_b32_e32 v1, 0x7c0
	s_load_dwordx8 s[4:11], s[0:1], 0x0
	s_load_dwordx2 s[18:19], s[0:1], 0x20
	s_load_dwordx2 s[28:29], s[0:1], 0x28
	s_load_dwordx2 s[34:35], s[0:1], 0x30
	s_load_dwordx2 s[30:31], s[0:1], 0x38
	v_med3_u32 v1, s14, 32, v1
	v_subrev_u32_e32 v97, 32, v1
	s_ashr_i32 s3, s2, 31
	v_lshlrev_b32_e32 v58, 1, v97
	s_lshl_b64 s[12:13], s[2:3], 12
	v_mov_b32_e32 v59, 0
	v_sub_u32_e32 v60, s14, v97
	v_lshl_add_u64 v[10:11], s[12:13], 0, v[58:59]
	v_lshlrev_b64 v[2:3], 9, v[10:11]
	v_lshl_or_b32 v22, v60, 6, v0
	s_waitcnt lgkmcnt(0)
	s_load_dword s32, s[28:29], 0x0
	v_and_b32_e32 v208, 31, v0
	v_lshlrev_b32_e32 v208, 5, v208
	global_load_dwordx4 v[192:195], v208, s[18:19]
	global_load_dwordx4 v[196:199], v208, s[18:19] offset:16
	v_lshl_add_u64 v[20:21], s[4:5], 0, v[2:3]
	v_ashrrev_i32_e32 v23, 31, v22
	v_lshl_add_u64 v[2:3], v[22:23], 4, v[20:21]
	global_load_dwordx4 v[12:15], v[2:3], off
	v_or_b32_e32 v28, 0x200, v22
	v_ashrrev_i32_e32 v29, 31, v28
	v_lshl_add_u64 v[2:3], v[28:29], 4, v[20:21]
	global_load_dwordx4 v[16:19], v[2:3], off
	v_or_b32_e32 v184, 0x400, v22
	v_ashrrev_i32_e32 v185, 31, v184
	v_lshl_add_u64 v[184:185], v[184:185], 4, v[20:21]
	v_or_b32_e32 v188, 0x600, v22
	v_ashrrev_i32_e32 v189, 31, v188
	v_lshl_add_u64 v[188:189], v[188:189], 4, v[20:21]
	global_load_dwordx4 v[184:187], v[184:185], off
	global_load_dwordx4 v[188:191], v[188:189], off
	v_lshrrev_b32_e32 v99, 6, v0
	v_and_b32_e32 v98, 63, v0
	v_lshlrev_b32_e32 v118, 13, v99
	v_lshl_or_b32 v58, v98, 5, v118
	s_movk_i32 s15, 0x1000
	v_lshl_add_u64 v[24:25], s[6:7], 0, v[58:59]
	v_or_b32_e32 v32, 0x400, v22
	v_or_b32_e32 v62, 0x600, v22
	v_add_co_u32_e32 v64, vcc, s15, v24
	s_mov_b64 s[12:13], 0x1000
	s_mov_b64 s[16:17], 0x1800
	v_lshlrev_b32_e32 v72, 1, v60
	v_lshrrev_b32_e32 v23, 5, v22
	v_and_b32_e32 v34, 32, v22
	v_ashrrev_i32_e32 v33, 31, v32
	v_ashrrev_i32_e32 v63, 31, v62
	v_addc_co_u32_e32 v65, vcc, 0, v25, vcc
	global_load_dwordx4 v[6:9], v58, s[6:7] offset:16
	global_load_dwordx4 v[2:5], v58, s[6:7]
	global_load_dwordx4 v[54:57], v58, s[6:7] offset:2064
	global_load_dwordx4 v[50:53], v58, s[6:7] offset:2048
	v_lshrrev_b32_e32 v58, 6, v22
	v_bfe_u32 v73, v22, 8, 2
	v_lshl_add_u64 v[26:27], v[24:25], 0, s[12:13]
	v_lshl_add_u64 v[24:25], v[24:25], 0, s[16:17]
	v_cmp_ne_u32_e32 vcc, 0, v34
	v_sub_u32_e32 v75, v23, v72
	global_load_dwordx4 v[42:45], v[64:65], off
	global_load_dwordx4 v[46:49], v[26:27], off offset:16
	global_load_dwordx4 v[34:37], v[64:65], off offset:2048
	global_load_dwordx4 v[38:41], v[24:25], off offset:16
	v_mov_b32_e32 v61, 0x60
	v_cndmask_b32_e32 v74, 0, v61, vcc
	v_add_u32_e32 v33, v74, v58
	v_lshlrev_b32_e32 v64, 2, v33
	v_bfe_u32 v96, v0, 4, 1
	v_and_b32_e32 v100, 15, v0
	v_mov_b32_e32 v30, v59
	v_mov_b32_e32 v31, v59
	v_and_b32_e32 v64, 12, v64
	v_mul_u32_u24_e32 v29, 0xc000, v96
	v_bitop3_b32 v64, v64, v100, v73 bitop3:0x36
	v_lshl_or_b32 v64, v64, 4, v29
	v_lshlrev_b32_e32 v63, 1, v75
	v_lshl_add_u32 v33, v33, 8, v64
	v_bfe_u32 v71, v0, 1, 4
	v_and_b32_e32 v70, 32, v0
	v_lshlrev_b32_e32 v1, 3, v0
	v_lshrrev_b32_e32 v58, 1, v75
	v_and_b32_e32 v1, 8, v1
	v_add_lshl_u32 v58, v58, v70, 8
	v_lshlrev_b32_e32 v121, 3, v99
	v_bfe_u32 v101, v0, 4, 2
	v_lshlrev_b32_e32 v102, 2, v101
	v_and_b32_e32 v116, 31, v0
	v_bfe_u32 v119, v0, 5, 1
	v_lshlrev_b32_e32 v124, 1, v119
	v_lshlrev_b32_e32 v117, 8, v116
	v_lshrrev_b32_e32 v95, 4, v0
	s_movk_i32 s16, 0x60
	s_mov_b32 s17, 0xc000
	v_and_b32_e32 v211, 3, v99
	v_lshrrev_b32_e32 v212, 2, v99
	v_lshl_or_b32 v211, v211, 2, v212
	v_xor_b32_e32 v213, v100, v211
	v_mul_u32_u24_e32 v214, 0x60, v119
	v_add3_u32 v214, v214, v60, v99
	v_mul_u32_u24_e32 v215, 0xc000, v96
	v_lshl_add_u32 v214, v214, 8, v215
	v_lshl_or_b32 v220, v213, 4, v214
	v_xor_b32_e32 v221, 32, v220
	v_xor_b32_e32 v216, v71, v211
	v_lshl_add_u32 v217, v119, 5, v99
	v_lshlrev_b32_e32 v217, 8, v217
	v_lshl_or_b32 v216, v216, 4, v217
	v_or_b32_e32 v216, v216, v1
	v_add_u32_e32 v222, 0x23800, v216
	v_xor_b32_e32 v223, 32, v222
	s_waitcnt vmcnt(11)
	ds_write_b128 v220, v[12:15]
	v_fma_mix_f32 v200, v192, v12, 0 op_sel_hi:[0,1,0]
	v_fma_mix_f32 v201, v193, v12, 0 op_sel:[0,1,0] op_sel_hi:[0,1,0]
	v_cvt_f32_f16_e32 v211, v12
	v_cvt_f32_f16_sdwa v212, v12 dst_sel:DWORD dst_unused:UNUSED_PAD src0_sel:WORD_1
	v_fma_mix_f32 v200, v194, v13, v200 op_sel_hi:[0,1,0]
	v_fma_mix_f32 v201, v195, v13, v201 op_sel:[0,1,0] op_sel_hi:[0,1,0]
	v_cvt_f32_f16_e32 v213, v13
	v_cvt_f32_f16_sdwa v214, v13 dst_sel:DWORD dst_unused:UNUSED_PAD src0_sel:WORD_1
	v_fma_mix_f32 v200, v196, v14, v200 op_sel_hi:[0,1,0]
	v_fma_mix_f32 v201, v197, v14, v201 op_sel:[0,1,0] op_sel_hi:[0,1,0]
	v_cvt_f32_f16_e32 v215, v14
	v_cvt_f32_f16_sdwa v216, v14 dst_sel:DWORD dst_unused:UNUSED_PAD src0_sel:WORD_1
	v_fma_mix_f32 v200, v198, v15, v200 op_sel_hi:[0,1,0]
	v_fma_mix_f32 v201, v199, v15, v201 op_sel:[0,1,0] op_sel_hi:[0,1,0]
	v_cvt_f32_f16_e32 v217, v15
	v_cvt_f32_f16_sdwa v218, v15 dst_sel:DWORD dst_unused:UNUSED_PAD src0_sel:WORD_1
	v_cvt_pk_fp8_f32 v224, v211, v212
	v_cvt_pk_fp8_f32 v225, v215, v216
	v_cvt_pk_fp8_f32 v224, v213, v214 op_sel:[0,0,1]
	v_cvt_pk_fp8_f32 v225, v217, v218 op_sel:[0,0,1]
	s_nop 0
	ds_write_b64 v222, v[224:225]
	s_waitcnt vmcnt(10)
	ds_write_b128 v221, v[16:19] offset:2048
	v_fma_mix_f32 v202, v192, v16, 0 op_sel_hi:[0,1,0]
	v_fma_mix_f32 v203, v193, v16, 0 op_sel:[0,1,0] op_sel_hi:[0,1,0]
	v_cvt_f32_f16_e32 v211, v16
	v_cvt_f32_f16_sdwa v212, v16 dst_sel:DWORD dst_unused:UNUSED_PAD src0_sel:WORD_1
	v_fma_mix_f32 v202, v194, v17, v202 op_sel_hi:[0,1,0]
	v_fma_mix_f32 v203, v195, v17, v203 op_sel:[0,1,0] op_sel_hi:[0,1,0]
	v_cvt_f32_f16_e32 v213, v17
	v_cvt_f32_f16_sdwa v214, v17 dst_sel:DWORD dst_unused:UNUSED_PAD src0_sel:WORD_1
	v_fma_mix_f32 v202, v196, v18, v202 op_sel_hi:[0,1,0]
	v_fma_mix_f32 v203, v197, v18, v203 op_sel:[0,1,0] op_sel_hi:[0,1,0]
	v_cvt_f32_f16_e32 v215, v18
	v_cvt_f32_f16_sdwa v216, v18 dst_sel:DWORD dst_unused:UNUSED_PAD src0_sel:WORD_1
	v_fma_mix_f32 v202, v198, v19, v202 op_sel_hi:[0,1,0]
	v_fma_mix_f32 v203, v199, v19, v203 op_sel:[0,1,0] op_sel_hi:[0,1,0]
	v_cvt_f32_f16_e32 v217, v19
	v_cvt_f32_f16_sdwa v218, v19 dst_sel:DWORD dst_unused:UNUSED_PAD src0_sel:WORD_1
	v_cvt_pk_fp8_f32 v226, v211, v212
	v_cvt_pk_fp8_f32 v227, v215, v216
	v_cvt_pk_fp8_f32 v226, v213, v214 op_sel:[0,0,1]
	v_cvt_pk_fp8_f32 v227, v217, v218 op_sel:[0,0,1]
	s_nop 0
	ds_write_b64 v223, v[226:227] offset:2048
	s_waitcnt vmcnt(9)
	ds_write_b128 v220, v[184:187] offset:4096
	v_fma_mix_f32 v204, v192, v184, 0 op_sel_hi:[0,1,0]
	v_fma_mix_f32 v205, v193, v184, 0 op_sel:[0,1,0] op_sel_hi:[0,1,0]
	v_cvt_f32_f16_e32 v211, v184
	v_cvt_f32_f16_sdwa v212, v184 dst_sel:DWORD dst_unused:UNUSED_PAD src0_sel:WORD_1
	v_fma_mix_f32 v204, v194, v185, v204 op_sel_hi:[0,1,0]
	v_fma_mix_f32 v205, v195, v185, v205 op_sel:[0,1,0] op_sel_hi:[0,1,0]
	v_cvt_f32_f16_e32 v213, v185
	v_cvt_f32_f16_sdwa v214, v185 dst_sel:DWORD dst_unused:UNUSED_PAD src0_sel:WORD_1
	v_fma_mix_f32 v204, v196, v186, v204 op_sel_hi:[0,1,0]
	v_fma_mix_f32 v205, v197, v186, v205 op_sel:[0,1,0] op_sel_hi:[0,1,0]
	v_cvt_f32_f16_e32 v215, v186
	v_cvt_f32_f16_sdwa v216, v186 dst_sel:DWORD dst_unused:UNUSED_PAD src0_sel:WORD_1
	v_fma_mix_f32 v204, v198, v187, v204 op_sel_hi:[0,1,0]
	v_fma_mix_f32 v205, v199, v187, v205 op_sel:[0,1,0] op_sel_hi:[0,1,0]
	v_cvt_f32_f16_e32 v217, v187
	v_cvt_f32_f16_sdwa v218, v187 dst_sel:DWORD dst_unused:UNUSED_PAD src0_sel:WORD_1
	v_cvt_pk_fp8_f32 v228, v211, v212
	v_cvt_pk_fp8_f32 v229, v215, v216
	v_cvt_pk_fp8_f32 v228, v213, v214 op_sel:[0,0,1]
	v_cvt_pk_fp8_f32 v229, v217, v218 op_sel:[0,0,1]
	s_nop 0
	ds_write_b64 v222, v[228:229] offset:4096
	s_waitcnt vmcnt(8)
	ds_write_b128 v221, v[188:191] offset:6144
	v_fma_mix_f32 v206, v192, v188, 0 op_sel_hi:[0,1,0]
	v_fma_mix_f32 v207, v193, v188, 0 op_sel:[0,1,0] op_sel_hi:[0,1,0]
	v_cvt_f32_f16_e32 v211, v188
	v_cvt_f32_f16_sdwa v212, v188 dst_sel:DWORD dst_unused:UNUSED_PAD src0_sel:WORD_1
	v_fma_mix_f32 v206, v194, v189, v206 op_sel_hi:[0,1,0]
	v_fma_mix_f32 v207, v195, v189, v207 op_sel:[0,1,0] op_sel_hi:[0,1,0]
	v_cvt_f32_f16_e32 v213, v189
	v_cvt_f32_f16_sdwa v214, v189 dst_sel:DWORD dst_unused:UNUSED_PAD src0_sel:WORD_1
	v_fma_mix_f32 v206, v196, v190, v206 op_sel_hi:[0,1,0]
	v_fma_mix_f32 v207, v197, v190, v207 op_sel:[0,1,0] op_sel_hi:[0,1,0]
	v_cvt_f32_f16_e32 v215, v190
	v_cvt_f32_f16_sdwa v216, v190 dst_sel:DWORD dst_unused:UNUSED_PAD src0_sel:WORD_1
	v_fma_mix_f32 v206, v198, v191, v206 op_sel_hi:[0,1,0]
	v_fma_mix_f32 v207, v199, v191, v207 op_sel:[0,1,0] op_sel_hi:[0,1,0]
	v_cvt_f32_f16_e32 v217, v191
	v_cvt_f32_f16_sdwa v218, v191 dst_sel:DWORD dst_unused:UNUSED_PAD src0_sel:WORD_1
	v_cvt_pk_fp8_f32 v230, v211, v212
	v_cvt_pk_fp8_f32 v231, v215, v216
	v_cvt_pk_fp8_f32 v230, v213, v214 op_sel:[0,0,1]
	v_cvt_pk_fp8_f32 v231, v217, v218 op_sel:[0,0,1]
	s_nop 0
	ds_write_b64 v223, v[230:231] offset:6144
	v_add_f32_e32 v200, v200, v201
	v_add_f32_e32 v202, v202, v203
	v_add_f32_e32 v204, v204, v205
	v_add_f32_e32 v206, v206, v207
	v_lshlrev_b32_e32 v208, 7, v119
	v_lshl_add_u32 v208, v99, 2, v208
	v_add_u32_e32 v208, 0x27800, v208
	v_add_f32_dpp v200, v200, v200 quad_perm:[1,0,3,2] row_mask:0xf bank_mask:0xf
	v_add_f32_dpp v202, v202, v202 quad_perm:[1,0,3,2] row_mask:0xf bank_mask:0xf
	v_add_f32_dpp v204, v204, v204 quad_perm:[1,0,3,2] row_mask:0xf bank_mask:0xf
	v_add_f32_dpp v206, v206, v206 quad_perm:[1,0,3,2] row_mask:0xf bank_mask:0xf
	v_add_f32_dpp v200, v200, v200 quad_perm:[2,3,0,1] row_mask:0xf bank_mask:0xf
	v_add_f32_dpp v202, v202, v202 quad_perm:[2,3,0,1] row_mask:0xf bank_mask:0xf
	v_add_f32_dpp v204, v204, v204 quad_perm:[2,3,0,1] row_mask:0xf bank_mask:0xf
	v_add_f32_dpp v206, v206, v206 quad_perm:[2,3,0,1] row_mask:0xf bank_mask:0xf
	v_add_f32_dpp v200, v200, v200 row_half_mirror row_mask:0xf bank_mask:0xf
	v_add_f32_dpp v202, v202, v202 row_half_mirror row_mask:0xf bank_mask:0xf
	v_add_f32_dpp v204, v204, v204 row_half_mirror row_mask:0xf bank_mask:0xf
	v_add_f32_dpp v206, v206, v206 row_half_mirror row_mask:0xf bank_mask:0xf
	v_add_f32_dpp v200, v200, v200 row_mirror row_mask:0xf bank_mask:0xf
	v_add_f32_dpp v202, v202, v202 row_mirror row_mask:0xf bank_mask:0xf
	v_add_f32_dpp v204, v204, v204 row_mirror row_mask:0xf bank_mask:0xf
	v_add_f32_dpp v206, v206, v206 row_mirror row_mask:0xf bank_mask:0xf
	v_add_f32_dpp v200, v200, v200 row_bcast:15 row_mask:0xa bank_mask:0xf
	v_add_f32_dpp v202, v202, v202 row_bcast:15 row_mask:0xa bank_mask:0xf
	v_add_f32_dpp v204, v204, v204 row_bcast:15 row_mask:0xa bank_mask:0xf
	v_add_f32_dpp v206, v206, v206 row_bcast:15 row_mask:0xa bank_mask:0xf
	s_mov_b32 exec_lo, 0xffff0000
	s_mov_b32 exec_hi, 0xffff0000
	ds_write_b32 v208, v200
	ds_write_b32 v208, v202 offset:32
	ds_write_b32 v208, v204 offset:64
	ds_write_b32 v208, v206 offset:96
	s_mov_b64 exec, -1
	v_lshlrev_b32_e32 v201, 7, v99
	v_lshl_or_b32 v201, v119, 4, v201
	global_load_dwordx4 v[184:187], v201, s[10:11]
	global_load_dwordx4 v[188:191], v201, s[10:11] offset:32
	global_load_dwordx4 v[192:195], v201, s[10:11] offset:64
	global_load_dwordx4 v[196:199], v201, s[10:11] offset:96
	v_cmp_lt_i32_e32 vcc, v121, v60
	s_nop 0
	v_mov_b32_e32 v15, v59
	v_cndmask_b32_e64 v12, 32, 0, vcc
	v_add_u32_e32 v16, v12, v121
	v_or_b32_e32 v12, v16, v101
	v_lshlrev_b32_e32 v58, 1, v12
	v_lshrrev_b32_e32 v12, 5, v0
	v_and_b32_e32 v12, 2, v12
	v_bitop3_b32 v14, v102, v100, v12 bitop3:0x36
	v_lshl_add_u64 v[12:13], v[10:11], 0, v[58:59]
	v_lshlrev_b64 v[12:13], 9, v[12:13]
	v_lshlrev_b32_e32 v16, 8, v16
	v_lshl_add_u64 v[12:13], s[4:5], 0, v[12:13]
	v_lshlrev_b32_e32 v14, 4, v14
	v_readfirstlane_b32 s6, v16
	v_add_u32_e32 v17, 0xc000, v16
	v_lshl_add_u64 v[12:13], v[12:13], 0, v[14:15]
	s_mov_b32 m0, s6
	s_mov_b64 s[6:7], 0x100
	v_readfirstlane_b32 s12, v17
	global_load_lds_dwordx4 v[12:13], off
	v_lshl_add_u64 v[12:13], v[12:13], 0, s[6:7]
	s_mov_b32 m0, s12
	v_or_b32_e32 v58, 1, v58
	global_load_lds_dwordx4 v[12:13], off
	v_lshl_add_u64 v[12:13], v[10:11], 0, v[58:59]
	v_lshlrev_b64 v[12:13], 9, v[12:13]
	v_lshl_add_u64 v[12:13], s[4:5], 0, v[12:13]
	v_lshl_add_u64 v[12:13], v[12:13], 0, v[14:15]
	v_add_u32_e32 v14, 0x6000, v16
	v_bfe_u32 v61, v0, 2, 2
	v_readfirstlane_b32 s12, v14
	v_add_u32_e32 v14, 0x12000, v16
	s_mov_b32 m0, s12
	v_readfirstlane_b32 s12, v14
	global_load_lds_dwordx4 v[12:13], off
	v_lshl_add_u64 v[12:13], v[12:13], 0, s[6:7]
	s_mov_b32 m0, s12
	v_add_u32_e32 v18, 0x23800, v117
	global_load_lds_dwordx4 v[12:13], off
	v_or_b32_e32 v12, 4, v121
	v_cmp_lt_i32_e32 vcc, v12, v60
	s_nop 1
	v_cndmask_b32_e64 v13, 32, 0, vcc
	v_add_u32_e32 v16, v13, v12
	v_or_b32_e32 v13, v16, v101
	v_lshlrev_b32_e32 v58, 1, v13
	v_bfe_u32 v12, v12, 2, 2
	v_bitop3_b32 v14, v102, v100, v12 bitop3:0x36
	v_lshl_add_u64 v[12:13], v[10:11], 0, v[58:59]
	v_lshlrev_b64 v[12:13], 9, v[12:13]
	v_lshlrev_b32_e32 v16, 8, v16
	v_lshl_add_u64 v[12:13], s[4:5], 0, v[12:13]
	v_lshlrev_b32_e32 v14, 4, v14
	v_readfirstlane_b32 s12, v16
	v_add_u32_e32 v17, 0xc000, v16
	v_lshl_add_u64 v[12:13], v[12:13], 0, v[14:15]
	s_mov_b32 m0, s12
	v_readfirstlane_b32 s12, v17
	v_or_b32_e32 v58, 1, v58
	global_load_lds_dwordx4 v[12:13], off
	v_lshl_add_u64 v[12:13], v[12:13], 0, s[6:7]
	s_mov_b32 m0, s12
	v_lshl_add_u64 v[10:11], v[10:11], 0, v[58:59]
	global_load_lds_dwordx4 v[12:13], off
	v_lshlrev_b64 v[10:11], 9, v[10:11]
	v_add_u32_e32 v12, 0x6000, v16
	v_lshl_add_u64 v[10:11], s[4:5], 0, v[10:11]
	v_readfirstlane_b32 s4, v12
	v_add_u32_e32 v12, 0x12000, v16
	v_lshl_add_u64 v[10:11], v[10:11], 0, v[14:15]
	s_mov_b32 m0, s4
	v_readfirstlane_b32 s4, v12
	global_load_lds_dwordx4 v[10:11], off
	v_lshl_add_u64 v[10:11], v[10:11], 0, s[6:7]
	s_mov_b32 m0, s4
	s_nop 0
	global_load_lds_dwordx4 v[10:11], off
	s_waitcnt lgkmcnt(0)
	s_barrier
	v_lshlrev_b32_e32 v10, 2, v0
	v_and_b32_e32 v94, 12, v10
	v_or_b32_e32 v120, v94, v61
	v_bitop3_b32 v10, v124, v94, v61 bitop3:0x1e
	v_lshl_or_b32 v14, v10, 4, v18
	v_bitop3_b32 v10, v124, v120, 1 bitop3:0x36
	v_lshl_or_b32 v19, v10, 4, v18
	ds_read_b128 v[10:13], v14
	ds_read_b128 v[62:65], v14 offset:8192
	ds_read_b128 v[14:17], v19
	ds_read_b128 v[66:69], v19 offset:8192
	v_bitop3_b32 v19, v124, v120, 4 bitop3:0x36
	v_lshl_or_b32 v19, v19, 4, v18
	v_bitop3_b32 v20, v124, v120, 5 bitop3:0x36
	v_lshl_or_b32 v20, v20, 4, v18
	ds_read_b128 v[70:73], v19
	ds_read_b128 v[78:81], v19 offset:8192
	ds_read_b128 v[74:77], v20
	ds_read_b128 v[82:85], v20 offset:8192
	v_bitop3_b32 v19, v124, v120, 8 bitop3:0x36
	v_lshl_or_b32 v19, v19, 4, v18
	v_bitop3_b32 v20, v124, v120, 9 bitop3:0x36
	v_lshl_or_b32 v20, v20, 4, v18
	ds_read_b128 v[86:89], v19
	ds_read_b128 v[104:107], v19 offset:8192
	ds_read_b128 v[90:93], v20
	ds_read_b128 v[108:111], v20 offset:8192
	v_bitop3_b32 v19, v124, v120, 12 bitop3:0x36
	v_lshl_or_b32 v19, v19, 4, v18
	v_bitop3_b32 v20, v124, v120, 13 bitop3:0x36
	v_lshl_or_b32 v18, v20, 4, v18
	ds_read_b128 v[126:129], v19
	ds_read_b128 v[134:137], v19 offset:8192
	ds_read_b128 v[130:133], v18
	ds_read_b128 v[138:141], v18 offset:8192
	v_mov_b32_e32 v103, 0x7f
	v_lshlrev_b32_e32 v58, 7, v99
	v_or_b32_e32 v122, 0x18000, v117
	s_waitcnt vmcnt(18) lgkmcnt(0)
	v_mfma_scale_f32_32x32x64_f8f6f4 v[18:33], v[2:9], v[10:17], 0, v103, v103 op_sel_hi:[0,0,0]
	v_lshlrev_b32_e32 v125, 3, v119
	v_or_b32_e32 v123, 0x1a000, v117
	v_mfma_scale_f32_32x32x64_f8f6f4 v[2:17], v[2:9], v[62:69], 0, v103, v103 op_sel_hi:[0,0,0]
	v_and_b32_e32 v62, 12, v95
	s_waitcnt vmcnt(16)
	v_mfma_scale_f32_32x32x64_f8f6f4 v[18:33], v[50:57], v[70:77], v[18:33], v103, v103 op_sel_hi:[0,0,0]
	v_mfma_scale_f32_32x32x64_f8f6f4 v[2:17], v[50:57], v[78:85], v[2:17], v103, v103 op_sel_hi:[0,0,0]
	s_brev_b32 s10, 60
	v_lshlrev_b32_e32 v58, 6, v0
	v_and_b32_e32 v58, 0x4000, v58
	v_or3_b32 v63, v122, v58, v125
	v_or3_b32 v58, v123, v58, v125
	s_waitcnt vmcnt(14)
	v_mfma_scale_f32_32x32x64_f8f6f4 v[18:33], v[42:49], v[86:93], v[18:33], v103, v103 op_sel_hi:[0,0,0]
	v_mfma_scale_f32_32x32x64_f8f6f4 v[2:17], v[42:49], v[104:111], v[2:17], v103, v103 op_sel_hi:[0,0,0]
	s_nop 0
	s_waitcnt vmcnt(12)
	v_mfma_scale_f32_32x32x64_f8f6f4 v[2:17], v[34:41], v[134:141], v[2:17], v103, v103 op_sel_hi:[0,0,0]
	v_mfma_scale_f32_32x32x64_f8f6f4 v[18:33], v[34:41], v[126:133], v[18:33], v103, v103 op_sel_hi:[0,0,0]
	s_waitcnt vmcnt(8)
	s_nop 15
	s_nop 1
	v_fma_f32 v2, v2, s10, v184
	v_fma_f32 v3, v3, s10, v185
	v_fma_f32 v4, v4, s10, v186
	v_fma_f32 v5, v5, s10, v187
	v_cvt_pk_f16_f32 v2, v2, v3
	v_cvt_pk_f16_f32 v3, v4, v5
	v_bitop3_b32 v4, v95, v120, 12 bitop3:0x6c
	v_pk_fma_f32 v[18:19], v[18:19], s[10:11], v[184:185] op_sel_hi:[1,0,1]
	v_pk_fma_f32 v[20:21], v[20:21], s[10:11], v[186:187] op_sel_hi:[1,0,1]
	v_lshlrev_b32_e32 v4, 4, v4
	v_cvt_pk_f16_f32 v18, v18, v19
	v_cvt_pk_f16_f32 v19, v20, v21
	v_or_b32_e32 v5, v63, v4
	v_or_b32_e32 v4, v58, v4
	ds_write_b64 v5, v[18:19]
	ds_write_b64 v4, v[2:3]
	v_pk_fma_f32 v[2:3], v[22:23], s[10:11], v[188:189] op_sel_hi:[1,0,1]
	v_pk_fma_f32 v[4:5], v[6:7], s[10:11], v[188:189] op_sel_hi:[1,0,1]
	v_pk_fma_f32 v[6:7], v[24:25], s[10:11], v[190:191] op_sel_hi:[1,0,1]
	v_cvt_pk_f16_f32 v2, v2, v3
	v_cvt_pk_f16_f32 v3, v6, v7
	v_pk_fma_f32 v[6:7], v[8:9], s[10:11], v[190:191] op_sel_hi:[1,0,1]
	v_cvt_pk_f16_f32 v4, v4, v5
	v_cvt_pk_f16_f32 v5, v6, v7
	v_bitop3_b32 v6, v62, v120, 1 bitop3:0x36
	v_lshlrev_b32_e32 v6, 4, v6
	v_or_b32_e32 v7, v63, v6
	ds_write_b64 v7, v[2:3]
	v_or_b32_e32 v2, v58, v6
	ds_write_b64 v2, v[4:5]
	v_pk_fma_f32 v[2:3], v[26:27], s[10:11], v[192:193] op_sel_hi:[1,0,1]
	v_pk_fma_f32 v[6:7], v[28:29], s[10:11], v[194:195] op_sel_hi:[1,0,1]
	v_cvt_pk_f16_f32 v2, v2, v3
	v_pk_fma_f32 v[4:5], v[10:11], s[10:11], v[192:193] op_sel_hi:[1,0,1]
	v_cvt_pk_f16_f32 v3, v6, v7
	v_pk_fma_f32 v[6:7], v[12:13], s[10:11], v[194:195] op_sel_hi:[1,0,1]
	v_cvt_pk_f16_f32 v4, v4, v5
	v_cvt_pk_f16_f32 v5, v6, v7
	v_bitop3_b32 v6, v62, v120, 2 bitop3:0x36
	v_lshlrev_b32_e32 v6, 4, v6
	v_or_b32_e32 v7, v63, v6
	ds_write_b64 v7, v[2:3]
	v_or_b32_e32 v2, v58, v6
	ds_write_b64 v2, v[4:5]
	v_pk_fma_f32 v[2:3], v[30:31], s[10:11], v[196:197] op_sel_hi:[1,0,1]
	v_pk_fma_f32 v[6:7], v[32:33], s[10:11], v[198:199] op_sel_hi:[1,0,1]
	v_cvt_pk_f16_f32 v2, v2, v3
	v_pk_fma_f32 v[4:5], v[14:15], s[10:11], v[196:197] op_sel_hi:[1,0,1]
	v_cvt_pk_f16_f32 v3, v6, v7
	v_pk_fma_f32 v[6:7], v[16:17], s[10:11], v[198:199] op_sel_hi:[1,0,1]
	v_cvt_pk_f16_f32 v4, v4, v5
	v_cvt_pk_f16_f32 v5, v6, v7
	v_bitop3_b32 v6, v62, v120, 3 bitop3:0x36
	v_lshlrev_b32_e32 v6, 4, v6
	v_or_b32_e32 v7, v63, v6
	ds_write_b64 v7, v[2:3]
	v_or_b32_e32 v2, v58, v6
	ds_write_b64 v2, v[4:5]
	s_waitcnt vmcnt(0) lgkmcnt(0)
	s_barrier
	v_and_b32_e32 v236, 1, v101
	v_lshrrev_b32_e32 v237, 1, v101
	v_xor_b32_e32 v237, v237, v236
	v_lshl_or_b32 v236, v236, 1, v237
	v_lshrrev_b32_e32 v27, 8, v0
	v_lshrrev_b32_e32 v3, 3, v0
	v_and_b32_e32 v3, 16, v3
	v_mul_u32_u24_e32 v28, 0x60, v27
	v_lshlrev_b32_e32 v26, 5, v27
	v_or_b32_e32 v146, v3, v100
	v_or_b32_e32 v147, v28, v100
	v_or_b32_e32 v4, v146, v26
	v_lshlrev_b32_e32 v209, 2, v4
	v_add_u32_e32 v209, 0x27800, v209
	v_lshlrev_b32_e32 v4, 8, v4
	v_bitop3_b32 v11, v236, v120, 12 bitop3:0x36
	v_or_b32_e32 v95, 0x1c000, v4
	v_lshlrev_b32_e32 v29, 3, v101
	v_bitop3_b32 v10, v236, v120, 8 bitop3:0x36
	v_lshlrev_b32_e32 v94, 4, v11
	v_lshlrev_b32_e32 v58, 4, v10
	v_bfe_u32 v103, v0, 6, 1
	v_xor_b32_e32 v238, v236, v120
	v_lshlrev_b32_e32 v238, 4, v238
	v_or_b32_e32 v239, v146, v26
	v_lshlrev_b32_e32 v239, 8, v239
	v_add_u32_e32 v239, 0x18000, v239
	v_or_b32_e32 v240, v239, v238
	v_xor_b32_e32 v241, 64, v240
	v_xor_b32_e32 v242, 0x80, v240
	v_xor_b32_e32 v243, 0xc0, v240
	v_mad_u32_u24 v239, v103, 48, v147
	v_lshlrev_b32_e32 v239, 8, v239
	v_or_b32_e32 v244, v239, v238
	v_xor_b32_e32 v245, 64, v244
	v_xor_b32_e32 v246, 0x80, v244
	v_xor_b32_e32 v247, 0xc0, v244
	ds_read_b32 v210, v209
	ds_read_b128 v[134:137], v240
	ds_read_b128 v[138:141], v241
	ds_read_b128 v[142:145], v242
	ds_read_b128 v[148:151], v243
	ds_read_b128 v[152:155], v240 offset:16384
	ds_read_b128 v[156:159], v241 offset:16384
	ds_read_b128 v[160:163], v242 offset:16384
	ds_read_b128 v[164:167], v243 offset:16384
	ds_read_b128 v[168:171], v244
	ds_read_b128 v[172:175], v245
	ds_read_b128 v[176:179], v246
	ds_read_b128 v[180:183], v247
	ds_read_b128 v[184:187], v244 offset:49152
	ds_read_b128 v[188:191], v245 offset:49152
	ds_read_b128 v[192:195], v246 offset:49152
	s_waitcnt lgkmcnt(6)
	v_mfma_f32_16x16x32_f16 v[110:113], v[168:171], v[134:137], 0
	ds_read_b128 v[196:199], v247 offset:49152
	s_movk_i32 s5, 0x2000
	v_mad_u32_u24 v44, v103, 48, v147
	v_lshlrev_b32_e32 v60, 8, v44
	s_waitcnt lgkmcnt(6)
	v_mfma_f32_16x16x32_f16 v[110:113], v[172:175], v[138:141], v[110:113]
	ds_read_b128 v[200:203], v244 offset:4096
	v_lshlrev_b32_e32 v44, 2, v44
	v_or_b32_e32 v35, v95, v58
	v_lshlrev_b32_e32 v58, 14, v99
	s_waitcnt lgkmcnt(6)
	v_mfma_f32_16x16x32_f16 v[110:113], v[176:179], v[142:145], v[110:113]
	ds_read_b128 v[204:207], v245 offset:4096
	v_and_b32_e32 v44, 12, v44
	v_or_b32_e32 v56, v44, v61
	v_bitop3_b32 v44, v236, v44, v61 bitop3:0x1e
	s_waitcnt lgkmcnt(6)
	v_mfma_f32_16x16x32_f16 v[110:113], v[180:183], v[148:151], v[110:113]
	ds_read_b128 v[212:215], v246 offset:4096
	v_lshl_add_u64 v[32:33], s[8:9], 0, v[58:59]
	v_lshlrev_b32_e32 v58, 4, v98
	v_or_b32_e32 v36, v95, v94
	s_waitcnt lgkmcnt(6)
	v_mfma_f32_16x16x32_f16 v[110:113], v[184:187], v[152:155], v[110:113]
	ds_read_b128 v[216:219], v247 offset:4096
	v_lshl_add_u64 v[88:89], v[32:33], 0, v[58:59]
	v_lshl_or_b32 v57, v44, 4, v60
	global_load_dwordx4 v[36:39], v[88:89], off
	s_waitcnt lgkmcnt(6)
	v_mfma_f32_16x16x32_f16 v[110:113], v[188:191], v[156:159], v[110:113]
	ds_read_b128 v[168:171], v244 offset:53248
	global_load_dwordx4 v[32:35], v[88:89], off offset:1024
	v_bitop3_b32 v48, v236, v56, 4 bitop3:0x36
	v_bitop3_b32 v64, v236, v56, 12 bitop3:0x36
	s_waitcnt lgkmcnt(6)
	v_mfma_f32_16x16x32_f16 v[110:113], v[192:195], v[160:163], v[110:113]
	ds_read_b128 v[172:175], v245 offset:53248
	v_mad_u32_u24 v104, v103, 3, 1
	v_lshlrev_b32_e32 v132, 4, v104
	v_add_u32_e32 v52, v132, v147
	s_waitcnt lgkmcnt(6)
	v_mfma_f32_16x16x32_f16 v[110:113], v[196:199], v[164:167], v[110:113]
	ds_read_b128 v[176:179], v246 offset:53248
	global_load_dwordx4 v[64:67], v[88:89], off offset:2048
	global_load_dwordx4 v[48:51], v[88:89], off offset:3072
	v_lshlrev_b32_e32 v60, 8, v52
	s_waitcnt lgkmcnt(6)
	v_mfma_f32_16x16x32_f16 v[126:129], v[200:203], v[134:137], 0
	ds_read_b128 v[180:183], v247 offset:53248
	v_lshlrev_b32_e32 v52, 2, v52
	v_and_b32_e32 v52, 12, v52
	v_or_b32_e32 v62, v52, v61
	s_waitcnt lgkmcnt(6)
	v_mfma_f32_16x16x32_f16 v[126:129], v[204:207], v[138:141], v[126:129]
	ds_read_b128 v[184:187], v244 offset:8192
	v_bitop3_b32 v52, v236, v52, v61 bitop3:0x1e
	v_lshl_or_b32 v63, v52, 4, v60
	v_bitop3_b32 v56, v236, v62, 4 bitop3:0x36
	s_waitcnt lgkmcnt(6)
	v_mfma_f32_16x16x32_f16 v[126:129], v[212:215], v[142:145], v[126:129]
	ds_read_b128 v[188:191], v245 offset:8192
	v_lshl_or_b32 v84, v56, 4, v60
	v_bitop3_b32 v68, v236, v62, 8 bitop3:0x36
	v_lshl_or_b32 v85, v68, 4, v60
	s_waitcnt lgkmcnt(6)
	v_mfma_f32_16x16x32_f16 v[126:129], v[216:219], v[148:151], v[126:129]
	ds_read_b128 v[192:195], v246 offset:8192
	v_bitop3_b32 v62, v236, v62, 12 bitop3:0x36
	v_mad_u32_u24 v105, v103, 3, 2
	v_lshlrev_b32_e32 v133, 4, v105
	s_waitcnt lgkmcnt(6)
	v_mfma_f32_16x16x32_f16 v[126:129], v[168:171], v[152:155], v[126:129]
	ds_read_b128 v[196:199], v247 offset:8192
	v_add_co_u32_e32 v114, vcc, s15, v88
	s_nop 1
	v_addc_co_u32_e32 v115, vcc, 0, v89, vcc
	v_add_u32_e32 v60, v133, v147
	s_waitcnt lgkmcnt(6)
	v_mfma_f32_16x16x32_f16 v[126:129], v[172:175], v[156:159], v[126:129]
	ds_read_b128 v[200:203], v244 offset:57344
	v_lshlrev_b32_e32 v72, 8, v60
	v_lshlrev_b32_e32 v60, 2, v60
	v_and_b32_e32 v60, 12, v60
	s_waitcnt lgkmcnt(6)
	v_mfma_f32_16x16x32_f16 v[126:129], v[176:179], v[160:163], v[126:129]
	ds_read_b128 v[204:207], v245 offset:57344
	v_or_b32_e32 v68, v60, v61
	v_bitop3_b32 v60, v236, v60, v61 bitop3:0x1e
	v_lshl_or_b32 v69, v60, 4, v72
	s_waitcnt lgkmcnt(6)
	v_mfma_f32_16x16x32_f16 v[126:129], v[180:183], v[164:167], v[126:129]
	ds_read_b128 v[212:215], v246 offset:57344
	v_bitop3_b32 v70, v236, v68, 4 bitop3:0x36
	v_lshl_or_b32 v70, v70, 4, v72
	v_bitop3_b32 v71, v236, v68, 8 bitop3:0x36
	s_waitcnt lgkmcnt(6)
	v_mfma_f32_16x16x32_f16 v[16:19], v[184:187], v[134:137], 0
	ds_read_b128 v[216:219], v247 offset:57344
	v_lshl_or_b32 v71, v71, 4, v72
	v_bitop3_b32 v60, v236, v68, 12 bitop3:0x36
	v_lshl_or_b32 v68, v60, 4, v72
	s_waitcnt lgkmcnt(6)
	v_mfma_f32_16x16x32_f16 v[16:19], v[188:191], v[138:141], v[16:19]
	v_add_co_u32_e32 v44, vcc, s5, v88
	s_movk_i32 s5, 0x3000
	s_nop 1
	v_addc_co_u32_e32 v45, vcc, 0, v89, vcc
	s_waitcnt lgkmcnt(5)
	v_mfma_f32_16x16x32_f16 v[16:19], v[192:195], v[142:145], v[16:19]
	global_load_dwordx4 v[84:87], v[114:115], off offset:1024
	global_load_dwordx4 v[80:83], v[114:115], off offset:2048
	global_load_dwordx4 v[92:95], v[44:45], off offset:-4096
	s_waitcnt lgkmcnt(4)
	v_mfma_f32_16x16x32_f16 v[16:19], v[196:199], v[148:151], v[16:19]
	global_load_dwordx4 v[76:79], v[44:45], off
	global_load_dwordx4 v[72:75], v[44:45], off offset:1024
	global_load_dwordx4 v[68:71], v[44:45], off offset:2048
	s_waitcnt lgkmcnt(3)
	v_mfma_f32_16x16x32_f16 v[16:19], v[200:203], v[152:155], v[16:19]
	global_load_dwordx4 v[52:55], v[44:45], off offset:3072
	v_mov_b32_e32 v13, 0xff61b1e6
	v_add_co_u32_e32 v6, vcc, s5, v88
	s_waitcnt lgkmcnt(2)
	v_mfma_f32_16x16x32_f16 v[16:19], v[204:207], v[156:159], v[16:19]
	s_nop 1
	v_addc_co_u32_e32 v7, vcc, 0, v89, vcc
	global_load_dwordx4 v[88:91], v[114:115], off offset:3072
	global_load_dwordx4 v[60:63], v[6:7], off
	s_waitcnt lgkmcnt(1)
	v_mfma_f32_16x16x32_f16 v[16:19], v[212:215], v[160:163], v[16:19]
	global_load_dwordx4 v[56:59], v[6:7], off offset:1024
	global_load_dwordx4 v[44:47], v[6:7], off offset:2048
	global_load_dwordx4 v[40:43], v[6:7], off offset:3072
	s_waitcnt lgkmcnt(0)
	v_mfma_f32_16x16x32_f16 v[16:19], v[216:219], v[164:167], v[16:19]
	s_nop 0
	s_mov_b32 s5, 0xff61b1e6
	s_nop 0
	v_or_b32_e32 v3, s14, v146
	v_mov_b32_e32 v4, 0x7df
	v_med3_u32 v3, v3, 32, v4
	v_or_b32_e32 v4, v97, v102
	v_sub_u32_e32 v3, v4, v3
	v_add_f32_e32 v2, s32, v210
	v_add_u32_e32 v3, 32, v3
	v_mad_u32_u24 v4, v103, 48, v3
	s_movk_i32 s4, 0x41
	v_add_f32_e32 v5, v2, v110
	v_mul_f32_e32 v5, 0x3db8aa3b, v5
	v_cmp_gt_u32_e32 vcc, s4, v4
	v_add_u32_e32 v6, 1, v4
	v_add_f32_e32 v7, v2, v111
	v_cndmask_b32_e32 v5, v13, v5, vcc
	v_mul_f32_e32 v7, 0x3db8aa3b, v7
	v_cmp_gt_u32_e32 vcc, s4, v6
	v_add_u32_e32 v8, 2, v4
	v_add_f32_e32 v9, v2, v112
	v_cndmask_b32_e32 v6, v13, v7, vcc
	v_mul_f32_e32 v9, 0x3db8aa3b, v9
	v_cmp_gt_u32_e32 vcc, s4, v8
	v_add_u32_e32 v4, 3, v4
	v_max3_f32 v7, v5, s5, v6
	v_cndmask_b32_e32 v8, v13, v9, vcc
	v_add_f32_e32 v9, v2, v113
	v_mul_f32_e32 v9, 0x3db8aa3b, v9
	v_cmp_gt_u32_e32 vcc, s4, v4
	v_add_u32_e32 v11, v3, v132
	v_add_f32_e32 v12, v2, v127
	v_cndmask_b32_e32 v10, v13, v9, vcc
	v_max3_f32 v4, v7, v8, v10
	v_add_f32_e32 v7, v2, v126
	v_mul_f32_e32 v7, 0x3db8aa3b, v7
	v_cmp_gt_u32_e32 vcc, s4, v11
	v_add_u32_e32 v9, 1, v11
	v_mul_f32_e32 v12, 0x3db8aa3b, v12
	v_cndmask_b32_e32 v7, v13, v7, vcc
	v_cmp_gt_u32_e32 vcc, s4, v9
	v_add_f32_e32 v14, v2, v128
	v_mul_f32_e32 v14, 0x3db8aa3b, v14
	v_cndmask_b32_e32 v9, v13, v12, vcc
	v_add_u32_e32 v12, 2, v11
	v_cmp_gt_u32_e32 vcc, s4, v12
	v_add_u32_e32 v11, 3, v11
	v_add_u32_e32 v3, v3, v133
	v_cndmask_b32_e32 v12, v13, v14, vcc
	v_add_f32_e32 v14, v2, v129
	v_mul_f32_e32 v14, 0x3db8aa3b, v14
	v_cmp_gt_u32_e32 vcc, s4, v11
	v_add_f32_e32 v11, v2, v16
	v_mul_f32_e32 v11, 0x3db8aa3b, v11
	v_cndmask_b32_e32 v15, v13, v14, vcc
	v_cmp_gt_u32_e32 vcc, s4, v3
	v_add_u32_e32 v14, 1, v3
	v_add_f32_e32 v16, v2, v17
	v_cndmask_b32_e32 v11, v13, v11, vcc
	v_mul_f32_e32 v16, 0x3db8aa3b, v16
	v_cmp_gt_u32_e32 vcc, s4, v14
	v_add_f32_e32 v17, v2, v18
	v_max3_f32 v4, v4, v7, v9
	v_cndmask_b32_e32 v14, v13, v16, vcc
	v_add_u32_e32 v16, 2, v3
	v_mul_f32_e32 v17, 0x3db8aa3b, v17
	v_cmp_gt_u32_e32 vcc, s4, v16
	v_add_u32_e32 v3, 3, v3
	v_add_f32_e32 v2, v2, v19
	v_max3_f32 v4, v4, v12, v15
	v_cndmask_b32_e32 v16, v13, v17, vcc
	v_mul_f32_e32 v2, 0x3db8aa3b, v2
	v_cmp_gt_u32_e32 vcc, s4, v3
	v_max3_f32 v4, v4, v11, v14
	v_lshlrev_b32_e32 v126, 5, v99
	v_cndmask_b32_e32 v17, v13, v2, vcc
	v_max3_f32 v2, v4, v16, v17
	v_mov_b32_e32 v3, v2
	v_lshlrev_b32_e32 v127, 2, v119
	v_lshrrev_b32_e32 v4, 7, v0
	v_cmp_gt_u32_e32 vcc, 16, v98
	v_permlane16_swap_b32_e32 v3, v2
	v_max_f32_e32 v2, v2, v3
	v_mov_b32_e32 v3, v2
	s_nop 1
	v_permlane32_swap_b32_e32 v3, v2
	v_max_f32_e32 v13, v2, v3
	v_and_b32_e32 v2, 0x180, v0
	v_or_b32_e32 v2, 0x23400, v2
	v_lshlrev_b32_e32 v3, 2, v100
	s_and_saveexec_b64 s[4:5], vcc
	v_lshlrev_b32_e32 v18, 6, v103
	v_add3_u32 v18, v2, v18, v3
	ds_write_b32 v18, v13
	s_or_b64 exec, exec, s[4:5]
	v_lshlrev_b32_e32 v18, 4, v103
	v_bitop3_b32 v19, v18, 16, v100 bitop3:0x36
	v_lshl_add_u32 v2, v19, 2, v2
	s_waitcnt lgkmcnt(0)
	s_barrier
	ds_read_b32 v19, v2
	v_max_f32_e32 v13, v13, v13
	v_mul_u32_u24_e32 v20, 0xd00, v4
	v_or_b32_e32 v2, 1, v124
	s_waitcnt lgkmcnt(0)
	v_max_f32_e32 v19, v19, v19
	v_max_f32_e32 v19, v13, v19
	v_sub_f32_e32 v5, v5, v19
	v_exp_f32_e32 v5, v5
	v_sub_f32_e32 v6, v6, v19
	v_exp_f32_e32 v6, v6
	v_sub_f32_e32 v8, v8, v19
	v_mul_u32_u24_e32 v13, 0xd0, v100
	v_exp_f32_e32 v8, v8
	v_sub_f32_e32 v10, v10, v19
	v_add3_u32 v20, v13, v20, v29
	v_exp_f32_e32 v10, v10
	v_or_b32_e32 v22, 0x20000, v20
	v_add_f32_e32 v20, 0, v5
	v_add_f32_e32 v20, v20, v6
	v_add_f32_e32 v20, v20, v8
	v_add_f32_e32 v23, v20, v10
	v_cvt_pk_f16_f32 v21, v8, v10
	v_cvt_pk_f16_f32 v20, v5, v6
	v_mad_u32_u24 v5, v103, s16, v22
	ds_write_b64 v5, v[20:21]
	v_sub_f32_e32 v5, v7, v19
	v_exp_f32_e32 v5, v5
	v_sub_f32_e32 v6, v9, v19
	v_exp_f32_e32 v6, v6
	v_sub_f32_e32 v7, v12, v19
	v_exp_f32_e32 v7, v7
	v_sub_f32_e32 v8, v15, v19
	v_exp_f32_e32 v8, v8
	v_sub_f32_e32 v10, v11, v19
	v_add_f32_e32 v9, v23, v5
	v_exp_f32_e32 v10, v10
	v_sub_f32_e32 v11, v14, v19
	v_add_f32_e32 v9, v9, v6
	v_exp_f32_e32 v11, v11
	v_sub_f32_e32 v12, v16, v19
	v_add_f32_e32 v9, v9, v7
	v_exp_f32_e32 v12, v12
	v_sub_f32_e32 v14, v17, v19
	v_add_f32_e32 v9, v9, v8
	v_exp_f32_e32 v14, v14
	v_add_f32_e32 v9, v9, v10
	v_add_f32_e32 v9, v9, v11
	v_add_f32_e32 v9, v9, v12
	v_add_f32_e32 v9, v9, v14
	v_mov_b32_e32 v15, v9
	v_cvt_pk_f16_f32 v7, v7, v8
	v_cvt_pk_f16_f32 v6, v5, v6
	v_lshl_add_u32 v5, v104, 5, v22
	ds_write_b64 v5, v[6:7]
	v_permlane16_swap_b32_e32 v15, v9
	v_add_f32_e32 v5, v9, v15
	v_mov_b32_e32 v6, v5
	s_movk_i32 s7, 0xd00
	s_mov_b32 s6, 0x20000
	v_cvt_pk_f16_f32 v9, v12, v14
	v_cvt_pk_f16_f32 v8, v10, v11
	v_lshl_add_u32 v7, v105, 5, v22
	ds_write_b64 v7, v[8:9]
	v_permlane32_swap_b32_e32 v6, v5
	s_and_saveexec_b64 s[4:5], vcc
	s_cbranch_execz .LBB1_4
	v_lshlrev_b32_e32 v4, 5, v4
	v_or_b32_e32 v7, v18, v100
	v_lshlrev_b32_e32 v4, 2, v4
	v_lshlrev_b32_e32 v7, 2, v7
	s_mov_b32 s8, 0x23600
	v_add3_u32 v4, v7, v4, s8
	v_add_f32_e32 v5, v5, v6
	ds_write_b32 v4, v5
